# v30 + attention queue claims: returning atomic no longer waited for at issue; result picked up at first use
# baseline (speedup 1.0000x reference)
; #define LAS __attribute__((address_space(3)))
; __device__ __forceinline__ void qkt(f32x16& p0, f32x16& p1, const LAS unsigned char* Kb, const bf16x8 (&qr)[4], float cinit, int r32, int hi) {
;     const int sw = (r32 >> 1) & 7;
;     bf16x8 kf[8];
; #pragma unroll
;     for (int d0 = 0; d0 < 4; ++d0) {
;         unsigned ka = (unsigned)(uintptr_t)Kb + r32 * 128 + (((2 * d0 + hi) ^ sw) << 4); asm volatile("" : "+v"(ka));
;         kf[2 * d0] = *(const LAS bf16x8*)(uintptr_t)ka;
;         kf[2 * d0 + 1] = *(const LAS bf16x8*)(uintptr_t)(ka + 4096);
;     }
; #pragma unroll
;     for (int r = 0; r < 16; ++r) { p0[r] = cinit; p1[r] = cinit; }
;     __builtin_amdgcn_sched_barrier(0);
; #pragma unroll
;     for (int d0 = 0; d0 < 4; ++d0) {
;         p0 = __builtin_amdgcn_mfma_f32_32x32x16_bf16(kf[2 * d0], qr[d0], p0, 0, 0, 0);
;         p1 = __builtin_amdgcn_mfma_f32_32x32x16_bf16(kf[2 * d0 + 1], qr[d0], p1, 0, 0, 0);
;     }
;     ...
;             const int v2 = u - AT_NFOX - AT_NDIL, qb = 15 - v2 / 48, bh = v2 % 48, b = bh / 6, h = bh % 6, q0 = qb * 256;
;             const size_t rb = (size_t)b * S;
;             const bf16_t* Kb = proj + ((size_t)(40 + h) * NTOK + rb) * 64;
;             const bf16_t* Vb = proj + ((size_t)(46 + h) * NTOK + rb) * 64;
;             const int tw = q0 + 32 * wid, t = tw + r32;
;             const int jhi = (q0 + 254) >> 6, jhi_w = (tw + 30) >> 6, T = jhi + 1;
;             float P_run = 1.f; bool wdone = false;
;             int issued = 3; bool alldone = false;
;             for (int i = 0; i < T; ++i) {
;                 if (i > 0) {
;                     const int n = issued - 1 - i; AT_WAIT_BAR(2, n);
;                     int c = 0;
; #pragma unroll
;                     for (int k = 0; k < 8; ++k) c += flags[((i - 1) & 1) * 8 + k];
;                     alldone = (c == 8);
;                 }
;                 if (alldone) break;
;                 if (issued < T) { SB_ISSUE(issued); ++issued; }
;                 const int j = jhi - i, buf = i & 3;
;                 if (j <= jhi_w && !wdone) {
;                     f32x16 p0, p1;
;                     qkt(p0, p1, lds + L_K + buf * 8192, qr, 0.f, r32, hi);
;                     const bool diag = (64 * j + 63 >= tw);
;                     float gp[8];
.LBB0_419:
	v_mov_b32_e32 v148, v157
	v_mov_b32_e32 v170, 0
	s_waitcnt vmcnt(0)
	s_and_saveexec_b64 s[18:19], s[10:11]
	s_cbranch_execz .LBB0_423
	s_mov_b64 s[28:29], exec
	v_mbcnt_lo_u32_b32 v1, s28, 0
	v_mbcnt_hi_u32_b32 v1, s29, v1
	v_cmp_eq_u32_e32 vcc, 0, v1
	s_and_saveexec_b64 s[20:21], vcc
	s_cbranch_execz .LBB0_422
	s_bcnt1_i32_b64 s4, s[28:29]
	v_mov_b32_e32 v18, s4
	global_atomic_add v170, v35, v18, s[58:59] sc0
.LBB0_422:
	s_or_b64 exec, exec, s[20:21]
.LBB0_423:
	s_or_b64 exec, exec, s[18:19]
	s_cmpk_gt_i32 s73, 0x1ff
	s_cselect_b64 s[28:29], -1, 0
	v_and_b32_e32 v169, 31, v148
	v_ashrrev_i32_e32 v116, 5, v148
	s_mov_b64 s[18:19], -1
	s_and_b64 vcc, exec, s[28:29]
	s_cbranch_vccz .LBB0_431
	s_cmpk_gt_u32 s73, 0xaff
	s_cbranch_scc0 .LBB0_483
	s_add_i32 s4, s73, 0xf500
	s_and_b32 s5, s4, 0xffff
	s_mul_i32 s5, s5, 0xaaab
	s_lshr_b32 s5, s5, 21
	s_mul_i32 s14, s5, 48
	s_sub_i32 s4, s4, s14
	s_mul_i32 s14, s4, 0xab
	s_bfe_u32 s14, s14, 0x6000a
	s_mul_i32 s15, s14, 6
	s_sub_i32 s4, s4, s15
	s_and_b32 s4, s4, 0xff
	s_lshl_b32 s39, s5, 8
	s_lshl_b32 s5, s14, 12
	s_lshl_b32 s4, s4, 15
	s_add_i32 s4, s4, s5
	v_ashrrev_i32_e32 v1, 3, v148
	s_lshl_b32 s4, s4, 7
	v_add_u32_e32 v18, s41, v1
	s_add_i32 s5, s4, 0xa000000
	v_lshrrev_b32_e32 v19, 1, v18
	s_add_u32 s18, s96, s5
	v_xor_b32_e32 v20, v19, v148
	v_ashrrev_i32_e32 v19, 31, v18
	s_addc_u32 s19, s97, 0
	v_lshlrev_b64 v[18:19], 7, v[18:19]
	v_lshlrev_b32_e32 v20, 4, v20
	v_lshl_add_u64 v[18:19], s[18:19], 0, v[18:19]
	v_and_b32_e32 v34, 0x70, v20
	v_lshl_add_u64 v[86:87], v[18:19], 0, v[34:35]
	v_ashrrev_i32_e32 v18, 2, v148
	s_add_i32 s4, s4, 0xb800000
	v_add_u32_e32 v18, s42, v18
	s_add_u32 s20, s96, s4
	v_ashrrev_i32_e32 v19, 31, v18
	s_addc_u32 s21, s97, 0
	v_lshlrev_b64 v[18:19], 7, v[18:19]
	v_lshlrev_b32_e32 v20, 3, v148
	v_lshl_add_u64 v[18:19], s[20:21], 0, v[18:19]
	v_and_b32_e32 v20, 24, v20
	v_lshl_add_u64 v[18:19], s[26:27], 1, v[18:19]
	v_lshlrev_b32_e32 v34, 1, v20
	v_lshl_add_u64 v[88:89], v[18:19], 0, v[34:35]
	v_lshrrev_b32_e32 v18, 1, v148
	v_bitop3_b32 v19, v18, v116, 7 bitop3:0x6c
	v_lshlrev_b32_e32 v102, 4, v19
	v_add_u32_e32 v19, 2, v116
	v_bitop3_b32 v19, v19, v18, 7 bitop3:0x78
	s_sub_i32 s38, s2, s39
	v_lshlrev_b32_e32 v103, 4, v19
	v_add_u32_e32 v19, 4, v116
	s_add_i32 s4, s38, 0xf00
	v_bitop3_b32 v19, v19, v18, 7 bitop3:0x78
	v_or_b32_e32 v84, s4, v169
	s_add_i32 s4, s38, 0xf1e
	v_lshlrev_b32_e32 v104, 4, v19
	v_add_u32_e32 v19, 6, v116
	s_sub_i32 s30, 0xfc0, s39
	s_ashr_i32 s37, s4, 6
	v_bitop3_b32 v18, v19, v18, 7 bitop3:0x78
	v_bfe_u32 v19, v148, 2, 2
	s_mov_b32 s4, 0x3fffffc
	v_lshlrev_b32_e32 v105, 4, v18
	v_lshlrev_b32_e32 v18, 1, v148
	v_and_or_b32 v1, v1, s4, v19
	s_lshl_b32 s4, s30, 7
	v_and_b32_e32 v18, 32, v18
	v_lshlrev_b32_e32 v1, 6, v1
	s_add_i32 s66, s4, 0xffffa000
	v_or3_b32 v107, v18, v1, v20
	v_lshl_add_u64 v[18:19], v[86:87], 0, s[66:67]
	s_add_i32 s4, s24, 0x6000
	s_mov_b32 s5, m0
	s_mov_b32 m0, s4
	s_nop 0
	global_load_lds_dwordx4 v[18:19], off
	s_mov_b32 m0, s5
	v_lshl_add_u64 v[20:21], v[88:89], 0, s[66:67]
	s_add_i32 s4, s24, 0x12000
	s_mov_b32 s5, m0
	s_mov_b32 m0, s4
	s_nop 0
	global_load_lds_dwordx4 v[20:21], off
	s_mov_b32 m0, s5
	s_lshr_b32 s36, s30, 6
	s_addk_i32 s38, 0xec1
	v_lshlrev_b32_e32 v85, 7, v169
	v_lshlrev_b32_e32 v106, 2, v116
	v_cmp_gt_u32_e64 s[18:19], 32, v148
	s_cmp_gt_i32 s36, s37
	s_cbranch_scc1 .LBB0_458
	v_add_u32_e32 v1, 0, v85
	v_add_u32_e32 v22, v1, v102
	v_add_u32_e32 v26, v1, v103
	ds_read_b128 v[18:21], v22
	ds_read_b128 v[22:25], v22 offset:4096
	ds_read_b128 v[52:55], v26
	ds_read_b128 v[56:59], v26 offset:4096
	v_add_u32_e32 v26, v1, v104
	v_add_u32_e32 v1, v1, v105
	ds_read_b128 v[60:63], v26
	ds_read_b128 v[64:67], v26 offset:4096
	ds_read_b128 v[68:71], v1
	ds_read_b128 v[72:75], v1 offset:4096
	s_waitcnt lgkmcnt(7)
	v_mfma_f32_32x32x16_bf16 v[36:51], v[18:21], v[132:135], 0
	s_cmp_lt_i32 s30, s38
	s_mov_b64 s[20:21], -1
	s_waitcnt lgkmcnt(6)
	v_mfma_f32_32x32x16_bf16 v[18:33], v[22:25], v[132:135], 0
	s_waitcnt lgkmcnt(5)
	v_mfma_f32_32x32x16_bf16 v[36:51], v[52:55], v[136:139], v[36:51]
	s_waitcnt lgkmcnt(4)
	v_mfma_f32_32x32x16_bf16 v[18:33], v[56:59], v[136:139], v[18:33]
	s_waitcnt lgkmcnt(3)
	v_mfma_f32_32x32x16_bf16 v[36:51], v[60:63], v[140:143], v[36:51]
	s_waitcnt lgkmcnt(2)
	v_mfma_f32_32x32x16_bf16 v[18:33], v[64:67], v[140:143], v[18:33]
	s_waitcnt lgkmcnt(1)
	v_mfma_f32_32x32x16_bf16 v[36:51], v[68:71], v[144:147], v[36:51]
	s_waitcnt lgkmcnt(0)
	v_mfma_f32_32x32x16_bf16 v[18:33], v[72:75], v[144:147], v[18:33]
	s_nop 9
	v_exp_f32_e32 v97, v39
	v_exp_f32_e32 v95, v38
	v_exp_f32_e32 v96, v37
	v_exp_f32_e32 v94, v36
	v_exp_f32_e32 v93, v43
	v_exp_f32_e32 v92, v42
	v_exp_f32_e32 v91, v41
	v_exp_f32_e32 v90, v40
	v_exp_f32_e32 v82, v47
	v_exp_f32_e32 v83, v46
	v_exp_f32_e32 v81, v45
	v_exp_f32_e32 v80, v44
	v_exp_f32_e32 v79, v51
	v_exp_f32_e32 v78, v50
	v_exp_f32_e32 v77, v49
	v_exp_f32_e32 v76, v48
	v_exp_f32_e32 v75, v21
	v_exp_f32_e32 v74, v20
	v_exp_f32_e32 v73, v19
	v_exp_f32_e32 v72, v18
	v_exp_f32_e32 v71, v25
	v_exp_f32_e32 v70, v24
	v_exp_f32_e32 v69, v23
	v_exp_f32_e32 v68, v22
	v_exp_f32_e32 v67, v29
	v_exp_f32_e32 v66, v28
	v_exp_f32_e32 v65, v27
	v_exp_f32_e32 v64, v26
	v_exp_f32_e32 v63, v33
	v_exp_f32_e32 v62, v32
	v_exp_f32_e32 v34, v31
	v_exp_f32_e32 v1, v30
	s_cbranch_scc1 .LBB0_428
;     ...
;                     if (diag) { asm volatile("; stick-breaking: diagonal tile (masked)" ::: "memory"); SB_GROUPS(true) } else { SB_GROUPS(false) }
	v_add_f32_e32 v19, 1.0, v95
	v_rcp_f32_e32 v20, v19
	v_add_f32_e32 v19, 1.0, v96
	v_rcp_f32_e32 v21, v19
	v_add_f32_e32 v19, 1.0, v94
	v_rcp_f32_e32 v22, v19
	v_add_f32_e32 v19, 1.0, v93
	v_add_f32_e32 v18, 1.0, v97
	v_rcp_f32_e32 v23, v19
	v_add_f32_e32 v19, 1.0, v92
	v_rcp_f32_e32 v18, v18
	v_rcp_f32_e32 v24, v19
	v_add_f32_e32 v19, 1.0, v91
	v_rcp_f32_e32 v28, v19
	v_add_f32_e32 v19, 1.0, v90
	v_add_u32_e32 v56, s30, v106
	v_rcp_f32_e32 v30, v19
	v_or_b32_e32 v19, 3, v56
	v_add_u32_e32 v25, 10, v56
	v_cmp_lt_i32_e32 vcc, v19, v84
	v_add_u32_e32 v26, 11, v56
	v_add_u32_e32 v37, 26, v56
	v_cndmask_b32_e32 v19, 1.0, v18, vcc
	v_cmp_lt_i32_e32 vcc, v25, v84
	v_add_u32_e32 v40, 27, v56
	v_mov_b32_e32 v200, v19
	v_cndmask_b32_e32 v18, 1.0, v24, vcc
	v_or_b32_e32 v24, 2, v56
	v_cmp_lt_i32_e32 vcc, v24, v84
	v_add_f32_e32 v44, 1.0, v72
	v_rcp_f32_e32 v44, v44
	v_cndmask_b32_e32 v25, 1.0, v20, vcc
	v_cmp_lt_i32_e32 vcc, v26, v84
	v_or_b32_e32 v20, 1, v56
	v_add_f32_e32 v48, 1.0, v68
	v_cndmask_b32_e32 v24, 1.0, v23, vcc
	v_add_u32_e32 v23, 9, v56
	v_cmp_lt_i32_e32 vcc, v20, v84
	v_pk_mul_f32 v[26:27], v[18:19], v[24:25]
	v_mov_b32_e32 v25, v201
	v_cndmask_b32_e32 v21, 1.0, v21, vcc
	v_cmp_lt_i32_e32 vcc, v23, v84
	v_mov_b32_e32 v18, v27
	v_mov_b32_e32 v23, v27
	v_cndmask_b32_e32 v20, 1.0, v28, vcc
	v_pk_mul_f32 v[28:29], v[20:21], v[26:27]
	v_add_u32_e32 v20, 8, v56
	v_cmp_lt_i32_e32 vcc, v56, v84
	v_mov_b32_e32 v27, v24
	v_mov_b32_e32 v31, v29
	v_cndmask_b32_e32 v21, 1.0, v22, vcc
	v_cmp_lt_i32_e32 vcc, v20, v84
	v_mov_b32_e32 v22, v29
	v_pk_add_f32 v[24:25], v[24:25], v[26:27] neg_lo:[0,1] neg_hi:[0,1]
	v_cndmask_b32_e32 v20, 1.0, v30, vcc
	v_pk_mul_f32 v[20:21], v[20:21], v[28:29]
	v_mov_b32_e32 v29, v26
	v_mov_b32_e32 v26, v20
	v_mov_b32_e32 v27, v28
	v_mov_b32_e32 v30, v21
	v_pk_add_f32 v[26:27], v[28:29], v[26:27] neg_lo:[0,1] neg_hi:[0,1]
	v_add_f32_e32 v29, 1.0, v83
	v_pk_add_f32 v[22:23], v[22:23], v[30:31] neg_lo:[0,1] neg_hi:[0,1]
	v_rcp_f32_e32 v30, v29
	v_add_f32_e32 v29, 1.0, v81
	v_rcp_f32_e32 v31, v29
	v_add_f32_e32 v29, 1.0, v80
	v_rcp_f32_e32 v32, v29
	v_add_f32_e32 v29, 1.0, v79
	v_add_f32_e32 v28, 1.0, v82
	v_rcp_f32_e32 v33, v29
	v_add_f32_e32 v29, 1.0, v78
	v_rcp_f32_e32 v28, v28
	v_rcp_f32_e32 v36, v29
	v_add_f32_e32 v29, 1.0, v77
	v_rcp_f32_e32 v38, v29
	v_add_f32_e32 v29, 1.0, v76
	v_rcp_f32_e32 v39, v29
	v_add_u32_e32 v29, 19, v56
	v_cmp_lt_i32_e32 vcc, v29, v84
	v_pk_add_f32 v[18:19], v[200:201], v[18:19] neg_lo:[0,1] neg_hi:[0,1]
	v_rcp_f32_e32 v48, v48
	v_cndmask_b32_e32 v29, 1.0, v28, vcc
	v_cmp_lt_i32_e32 vcc, v37, v84
	v_mov_b32_e32 v200, v29
	v_add_u32_e32 v58, 58, v56
	v_cndmask_b32_e32 v28, 1.0, v36, vcc
	v_add_u32_e32 v36, 18, v56
	v_cmp_lt_i32_e32 vcc, v36, v84
	s_mov_b64 s[20:21], 0
	s_nop 0
	v_cndmask_b32_e32 v37, 1.0, v30, vcc
	v_cmp_lt_i32_e32 vcc, v40, v84
	v_add_u32_e32 v30, 17, v56
	s_nop 0
	v_cndmask_b32_e32 v36, 1.0, v33, vcc
	v_add_u32_e32 v33, 25, v56
	v_cmp_lt_i32_e32 vcc, v30, v84
	v_pk_mul_f32 v[40:41], v[28:29], v[36:37]
	v_mov_b32_e32 v37, v201
	v_cndmask_b32_e32 v31, 1.0, v31, vcc
	v_cmp_lt_i32_e32 vcc, v33, v84
	v_add_u32_e32 v33, 24, v56
	v_mov_b32_e32 v28, v41
	v_cndmask_b32_e32 v30, 1.0, v38, vcc
	v_pk_mul_f32 v[42:43], v[30:31], v[40:41]
	v_add_u32_e32 v30, 16, v56
	v_cmp_lt_i32_e32 vcc, v30, v84
	v_pk_add_f32 v[28:29], v[200:201], v[28:29] neg_lo:[0,1] neg_hi:[0,1]
	s_nop 0
	v_cndmask_b32_e32 v31, 1.0, v32, vcc
	v_cmp_lt_i32_e32 vcc, v33, v84
	s_nop 1
	v_cndmask_b32_e32 v30, 1.0, v39, vcc
	v_pk_mul_f32 v[32:33], v[30:31], v[42:43]
	v_mov_b32_e32 v30, v43
	v_mov_b32_e32 v31, v41
	v_mov_b32_e32 v38, v33
	v_mov_b32_e32 v39, v43
	v_mov_b32_e32 v41, v36
	v_pk_add_f32 v[30:31], v[30:31], v[38:39] neg_lo:[0,1] neg_hi:[0,1]
	v_pk_add_f32 v[38:39], v[36:37], v[40:41] neg_lo:[0,1] neg_hi:[0,1]
;     ...
;                     if (diag) { asm volatile("; stick-breaking: diagonal tile (masked)" ::: "memory"); SB_GROUPS(true) } else { SB_GROUPS(false) }
	v_mov_b32_e32 v43, v40
	v_mov_b32_e32 v36, v32
	v_mov_b32_e32 v37, v42
	v_pk_add_f32 v[36:37], v[42:43], v[36:37] neg_lo:[0,1] neg_hi:[0,1]
	v_add_f32_e32 v42, 1.0, v75
	v_rcp_f32_e32 v42, v42
	v_add_f32_e32 v43, 1.0, v74
	v_rcp_f32_e32 v43, v43
	v_add_u32_e32 v41, 35, v56
	v_cmp_lt_i32_e32 vcc, v41, v84
	v_add_u32_e32 v41, 34, v56
	v_add_u32_e32 v40, 32, v56
	v_cndmask_b32_e32 v200, 1.0, v42, vcc
	v_cmp_lt_i32_e32 vcc, v41, v84
	v_add_u32_e32 v42, 33, v56
	s_nop 0
	v_cndmask_b32_e32 v41, 1.0, v43, vcc
	v_add_f32_e32 v43, 1.0, v73
	v_rcp_f32_e32 v43, v43
	v_cmp_lt_i32_e32 vcc, v42, v84
	v_mul_f32_e32 v42, v200, v41
	v_mov_b32_e32 v47, v42
	v_cndmask_b32_e32 v45, 1.0, v43, vcc
	v_cmp_lt_i32_e32 vcc, v40, v84
	v_mul_f32_e32 v46, v45, v42
	v_mov_b32_e32 v43, v200
	v_cndmask_b32_e32 v44, 1.0, v44, vcc
	v_mul_f32_e32 v44, v44, v46
	v_mov_b32_e32 v45, v46
	v_pk_add_f32 v[40:41], v[200:201], v[42:43] neg_lo:[0,1] neg_hi:[0,1]
	v_pk_add_f32 v[42:43], v[46:47], v[44:45] neg_lo:[0,1] neg_hi:[0,1]
	v_add_f32_e32 v46, 1.0, v71
	v_rcp_f32_e32 v46, v46
	v_add_f32_e32 v47, 1.0, v70
	v_rcp_f32_e32 v47, v47
	v_add_u32_e32 v45, 43, v56
	v_cmp_lt_i32_e32 vcc, v45, v84
	v_add_u32_e32 v45, 42, v56
	s_nop 0
	v_cndmask_b32_e32 v200, 1.0, v46, vcc
	v_cmp_lt_i32_e32 vcc, v45, v84
	v_add_u32_e32 v46, 41, v56
	v_mov_b32_e32 v49, v200
	v_cndmask_b32_e32 v45, 1.0, v47, vcc
	v_add_f32_e32 v47, 1.0, v69
	v_rcp_f32_e32 v47, v47
	v_cmp_lt_i32_e32 vcc, v46, v84
	v_add_u32_e32 v46, 40, v56
	s_nop 0
	v_cndmask_b32_e32 v50, 1.0, v47, vcc
	v_cmp_lt_i32_e32 vcc, v46, v84
	s_nop 1
	v_cndmask_b32_e32 v51, 1.0, v48, vcc
	v_mul_f32_e32 v48, v200, v45
	v_mul_f32_e32 v52, v50, v48
	v_mul_f32_e32 v50, v51, v52
	v_mov_b32_e32 v53, v48
	v_mov_b32_e32 v51, v52
	v_pk_add_f32 v[46:47], v[200:201], v[48:49] neg_lo:[0,1] neg_hi:[0,1]
	v_pk_add_f32 v[48:49], v[52:53], v[50:51] neg_lo:[0,1] neg_hi:[0,1]
	v_add_f32_e32 v52, 1.0, v65
	v_rcp_f32_e32 v54, v52
	v_add_f32_e32 v52, 1.0, v64
	v_add_f32_e32 v45, 1.0, v67
	v_rcp_f32_e32 v57, v52
	v_add_f32_e32 v52, 1.0, v63
	v_rcp_f32_e32 v45, v45
	v_rcp_f32_e32 v55, v52
	v_add_f32_e32 v52, 1.0, v62
	v_add_f32_e32 v53, 1.0, v34
	v_add_f32_e32 v51, 1.0, v66
	v_rcp_f32_e32 v52, v52
	v_rcp_f32_e32 v60, v53
	v_add_f32_e32 v53, 1.0, v1
	v_rcp_f32_e32 v51, v51
	v_rcp_f32_e32 v61, v53
	v_add_u32_e32 v53, 51, v56
	v_cmp_lt_i32_e32 vcc, v53, v84
	s_nop 1
	v_cndmask_b32_e32 v53, 1.0, v45, vcc
	v_cmp_lt_i32_e32 vcc, v58, v84
	v_add_u32_e32 v45, 50, v56
	v_add_u32_e32 v58, 59, v56
	v_cndmask_b32_e32 v52, 1.0, v52, vcc
	v_cmp_lt_i32_e32 vcc, v45, v84
	v_add_u32_e32 v45, 49, v56
	v_mov_b32_e32 v200, v53
	v_cndmask_b32_e32 v59, 1.0, v51, vcc
	v_cmp_lt_i32_e32 vcc, v58, v84
	v_add_u32_e32 v51, 57, v56
	s_nop 0
	v_cndmask_b32_e32 v58, 1.0, v55, vcc
	v_cmp_lt_i32_e32 vcc, v45, v84
	v_add_u32_e32 v45, 48, v56
	v_pk_mul_f32 v[98:99], v[52:53], v[58:59]
	v_cndmask_b32_e32 v55, 1.0, v54, vcc
	v_cmp_lt_i32_e32 vcc, v51, v84
	v_add_u32_e32 v51, 56, v56
	v_mov_b32_e32 v52, v99
	v_cndmask_b32_e32 v54, 1.0, v60, vcc
	v_cmp_lt_i32_e32 vcc, v45, v84
	v_pk_mul_f32 v[100:101], v[54:55], v[98:99]
	v_mov_b32_e32 v59, v201
	v_cndmask_b32_e32 v55, 1.0, v57, vcc
	v_cmp_lt_i32_e32 vcc, v51, v84
	v_pk_add_f32 v[52:53], v[200:201], v[52:53] neg_lo:[0,1] neg_hi:[0,1]
	s_nop 0
	v_cndmask_b32_e32 v54, 1.0, v61, vcc
	v_pk_mul_f32 v[56:57], v[54:55], v[100:101]
	v_mov_b32_e32 v54, v101
	v_mov_b32_e32 v55, v99
	v_mov_b32_e32 v60, v57
	v_mov_b32_e32 v61, v101
	v_mov_b32_e32 v99, v58
	v_pk_add_f32 v[54:55], v[54:55], v[60:61] neg_lo:[0,1] neg_hi:[0,1]
	v_pk_add_f32 v[60:61], v[58:59], v[98:99] neg_lo:[0,1] neg_hi:[0,1]
	v_mov_b32_e32 v101, v98
	v_mov_b32_e32 v58, v56
	v_mov_b32_e32 v59, v100
	v_pk_add_f32 v[58:59], v[100:101], v[58:59] neg_lo:[0,1] neg_hi:[0,1]

;     ...
;         if (tid == 0) info[1] = AT_QMAP((int)nextu);
;         asm volatile("s_waitcnt vmcnt(0) lgkmcnt(0)\n\ts_barrier" ::: "memory");
;         const int un = info[1];
.LBB0_494:
	s_waitcnt vmcnt(0)
	v_add_u32_e32 v170, s77, v170
	s_movk_i32 s4, 0x200
	v_add_u32_e32 v34, 0x900, v170
	v_cmp_gt_i32_e32 vcc, s4, v170
	v_readlane_b32 s4, v253, 55
	s_nop 0
	v_cndmask_b32_e32 v34, v34, v170, vcc
	v_mov_b32_e32 v52, s4
	ds_write_b32 v52, v34

; __device__ __forceinline__ void at_dil(const Args& a, LAS unsigned char* lds, int layer) {
;     ...
;         if (tid == 0) nextu = __hip_atomic_fetch_add(queue, 1u, __ATOMIC_RELAXED, __HIP_MEMORY_SCOPE_AGENT);
;         const int twlo = wid >> 1;
;         u32x4 pw[3][4];
;         float l_part = 0.f, m_run = -INFINITY;
;         if (dil_fixed) {
; #pragma unroll
;             for (int j = 0; j < 3; ++j) {
;                 const int tt = twlo + 2 - j;
;                 if (tt >= tt_lo) {
;                     f32x16 p0, p1;
;                     qkt(p0, p1, lds + L_K + tt * 8192, qr, -m_dil, r32, hi);
.LBB0_553:
	v_mov_b32_e32 v34, 0
	s_and_saveexec_b64 s[20:21], s[4:5]
	s_cbranch_execz .LBB0_557
	s_mov_b64 s[24:25], exec
	v_mbcnt_lo_u32_b32 v18, s24, 0
	v_mbcnt_hi_u32_b32 v18, s25, v18
	v_cmp_eq_u32_e32 vcc, 0, v18
	s_and_saveexec_b64 s[22:23], vcc
	s_cbranch_execz .LBB0_556
	s_bcnt1_i32_b64 s24, s[24:25]
	v_mov_b32_e32 v19, s24
	global_atomic_add v34, v35, v19, s[12:13] sc0
.LBB0_556:
	s_or_b64 exec, exec, s[22:23]
.LBB0_557:
	s_or_b64 exec, exec, s[20:21]
	v_ashrrev_i32_e32 v57, 5, v135
	v_lshrrev_b32_e32 v18, 1, v135
	s_ashr_i32 s94, s78, 4
	v_bitop3_b32 v19, v18, v57, 7 bitop3:0x6c
	s_cmp_eq_u32 s94, 1
	v_lshlrev_b32_e32 v144, 4, v19
	v_add_u32_e32 v19, 2, v57
	s_cselect_b64 s[20:21], -1, 0
	v_bitop3_b32 v19, v19, v18, 7 bitop3:0x78
	s_and_b64 s[22:23], s[20:21], exec
	v_lshlrev_b32_e32 v142, 4, v19
	v_add_u32_e32 v19, 4, v57
	s_cselect_b32 s24, 2, 4
	s_and_b64 s[22:23], s[16:17], exec
	v_bitop3_b32 v19, v19, v18, 7 bitop3:0x78
	s_cselect_b32 s22, 0, s24
	v_lshlrev_b32_e32 v141, 4, v19
	v_add_u32_e32 v19, 6, v57
	s_lshr_b32 s95, s26, s22
	v_bitop3_b32 v18, v19, v18, 7 bitop3:0x78
	v_and_b32_e32 v136, 31, v135
	s_cmp_eq_u32 s95, 0
	v_lshlrev_b32_e32 v140, 4, v18
	v_lshlrev_b32_e32 v18, 2, v57
	s_cselect_b32 s54, 2, 0
	v_lshlrev_b32_e32 v143, 7, v136
	v_sub_u32_e32 v139, 0, v18
	s_mov_b64 s[24:25], 0
	s_and_saveexec_b64 s[22:23], s[6:7]
	s_xor_b64 s[22:23], exec, s[22:23]
	s_cbranch_execz .LBB0_562
	v_lshlrev_b32_e32 v18, 2, v136
	v_lshlrev_b32_e32 v19, 4, v57
	v_sub_u32_e32 v18, v18, v19
	v_add_u32_e32 v52, 0x4000, v140
	v_add_u32_e32 v53, s49, v143
	v_add_u32_e32 v54, 0x4000, v141
	v_add_u32_e32 v55, 0x4000, v142
	v_add_u32_e32 v56, 0x4000, v144
	s_mov_b32 s24, 2
	v_add_u32_e32 v57, s37, v18
	v_mov_b32_e32 v58, 0xff800000
	s_mov_b32 s25, 0
	s_branch .LBB0_560

; __device__ __forceinline__ void at_dil(const Args& a, LAS unsigned char* lds, int layer) {
;     ...
;         if (tid == 0) info[1] = (int)nextu;
;         asm volatile("s_waitcnt vmcnt(0) lgkmcnt(0)\n\ts_barrier" ::: "memory");
;         const int un2 = info[1];
.LBB0_578:
	s_waitcnt vmcnt(0)
	v_readlane_b32 s10, v253, 55
	s_nop 1
	v_mov_b32_e32 v18, s10
	ds_write_b32 v18, v34
